# baseline (speedup 1.0000x reference)
.Lmsk_8416:
	s_and_saveexec_b64 s[2:3], s[0:1]
	v_add_f32_e32 v34, v51, v34
	ds_write_b32 v223, v34 offset:49280
	s_or_b64 exec, exec, s[2:3]
	s_waitcnt lgkmcnt(0)
	ds_read_b128 v[34:37], v50 offset:49280
	ds_read_b128 v[38:41], v50 offset:49312
	s_lshl_b64 s[2:3], s[14:15], 1
	s_add_u32 s2, s10, s2
	s_addc_u32 s3, s11, s3
	s_waitcnt lgkmcnt(1)
	v_rcp_f32_e32 v42, v34
	v_rcp_f32_e32 v43, v35
	s_lshl_b32 s6, s34, 12
	s_add_i32 s6, s6, 0
	v_lshlrev_b32_e32 v230, 1, v222
	v_lshlrev_b32_e32 v231, 9, v211
	v_rcp_f32_e32 v44, v36
	v_rcp_f32_e32 v45, v37
	s_waitcnt lgkmcnt(0)
	v_rcp_f32_e32 v46, v38
	ds_read_b128 v[34:37], v50 offset:49344
	v_rcp_f32_e32 v47, v39
	v_rcp_f32_e32 v48, v40
	v_rcp_f32_e32 v49, v41
	ds_read_b128 v[38:41], v50 offset:49376
	v_add3_u32 v50, s6, v230, v231
	v_fma_mixlo_f16 v2, v2, v42, 0
	ds_write_b16 v50, v2 offset:51200
	v_fma_mixlo_f16 v2, v18, v42, 0
	ds_write_b16 v50, v2 offset:51264
	v_fma_mixlo_f16 v2, v3, v43, 0
	ds_write_b16 v50, v2 offset:51328
	v_fma_mixlo_f16 v2, v19, v43, 0
	ds_write_b16 v50, v2 offset:51392
	v_fma_mixlo_f16 v2, v4, v44, 0
	ds_write_b16 v50, v2 offset:51456
	v_fma_mixlo_f16 v2, v20, v44, 0
	ds_write_b16 v50, v2 offset:51520
	v_fma_mixlo_f16 v2, v5, v45, 0
	ds_write_b16 v50, v2 offset:51584
	v_fma_mixlo_f16 v2, v21, v45, 0
	ds_write_b16 v50, v2 offset:51648
	v_fma_mixlo_f16 v2, v6, v46, 0
	ds_write_b16 v50, v2 offset:52224
	v_fma_mixlo_f16 v2, v22, v46, 0
	ds_write_b16 v50, v2 offset:52288
	v_fma_mixlo_f16 v2, v7, v47, 0
	ds_write_b16 v50, v2 offset:52352
	v_fma_mixlo_f16 v2, v23, v47, 0
	s_waitcnt lgkmcnt(12)
	v_rcp_f32_e32 v34, v34
	ds_write_b16 v50, v2 offset:52416
	v_fma_mixlo_f16 v2, v8, v48, 0
	ds_write_b16 v50, v2 offset:52480
	v_fma_mixlo_f16 v2, v24, v48, 0
	v_rcp_f32_e32 v35, v35
	ds_write_b16 v50, v2 offset:52544
	v_fma_mixlo_f16 v2, v9, v49, 0
	ds_write_b16 v50, v2 offset:52608
	v_fma_mixlo_f16 v2, v25, v49, 0
	v_rcp_f32_e32 v36, v36
	ds_write_b16 v50, v2 offset:52672
	v_fma_mixlo_f16 v2, v10, v34, 0
	ds_write_b16 v50, v2 offset:53248
	v_fma_mixlo_f16 v2, v26, v34, 0
	v_rcp_f32_e32 v37, v37
	ds_write_b16 v50, v2 offset:53312
	v_fma_mixlo_f16 v2, v11, v35, 0
	ds_write_b16 v50, v2 offset:53376
	v_fma_mixlo_f16 v2, v27, v35, 0
	s_waitcnt lgkmcnt(14)
	v_rcp_f32_e32 v38, v38
	ds_write_b16 v50, v2 offset:53440
	v_fma_mixlo_f16 v2, v12, v36, 0
	ds_write_b16 v50, v2 offset:53504
	v_fma_mixlo_f16 v2, v28, v36, 0
	v_rcp_f32_e32 v39, v39
	ds_write_b16 v50, v2 offset:53568
	v_fma_mixlo_f16 v2, v13, v37, 0
	ds_write_b16 v50, v2 offset:53632
	v_fma_mixlo_f16 v2, v29, v37, 0
	v_rcp_f32_e32 v40, v40
	ds_write_b16 v50, v2 offset:53696
	v_fma_mixlo_f16 v2, v14, v38, 0
	ds_write_b16 v50, v2 offset:54272
	v_fma_mixlo_f16 v2, v30, v38, 0
	v_rcp_f32_e32 v41, v41
	ds_write_b16 v50, v2 offset:54336
	v_fma_mixlo_f16 v2, v15, v39, 0
	ds_write_b16 v50, v2 offset:54400
	v_fma_mixlo_f16 v2, v31, v39, 0
	ds_write_b16 v50, v2 offset:54464
	v_fma_mixlo_f16 v2, v16, v40, 0
	ds_write_b16 v50, v2 offset:54528
	v_fma_mixlo_f16 v2, v32, v40, 0
	ds_write_b16 v50, v2 offset:54592
	v_fma_mixlo_f16 v2, v17, v41, 0
	ds_write_b16 v50, v2 offset:54656
	v_fma_mixlo_f16 v2, v33, v41, 0
	ds_write_b16 v50, v2 offset:54720
	v_and_b32_e32 v2, 56, v209
	s_lshl_b32 s22, s33, 1
	v_lshrrev_b32_e32 v36, 3, v207
	v_lshlrev_b32_e32 v220, 1, v2
	s_add_u32 s2, s2, s22
	v_add_u32_e32 v14, s6, v220
	v_lshlrev_b32_e32 v232, 7, v36
	s_addc_u32 s3, s3, 0
	s_waitcnt lgkmcnt(0)
	v_mov_b32_e32 v221, 0
	v_add_u32_e32 v2, v14, v232
	v_or_b32_e32 v37, 8, v36
	v_lshl_add_u64 v[10:11], s[2:3], 0, v[220:221]
	ds_read_b128 v[2:5], v2 offset:51200
	v_lshlrev_b32_e32 v6, 11, v36
	v_mov_b32_e32 v7, v221
	v_lshlrev_b32_e32 v233, 7, v37
	v_readfirstlane_b32 s8, v0
	v_lshl_add_u64 v[12:13], v[10:11], 0, v[6:7]
	v_add_u32_e32 v6, v14, v233
	s_lshr_b32 s23, s8, 6
	ds_read_b128 v[6:9], v6 offset:51200
	s_or_b32 s2, s12, s27
	s_lshl_b32 s12, s23, 5
	s_add_u32 s6, s2, s12
	s_addc_u32 s7, s13, 0
	s_waitcnt lgkmcnt(1)
	global_store_dwordx4 v[12:13], v[2:5], off
	v_or_b32_e32 v38, 16, v36
	s_lshl_b64 s[2:3], s[6:7], 11
	v_lshlrev_b32_e32 v2, 11, v37
	v_mov_b32_e32 v3, v221
	v_lshl_add_u64 v[2:3], v[10:11], 0, v[2:3]
	v_lshlrev_b32_e32 v234, 7, v38
	s_add_u32 s2, s4, s2
	s_waitcnt lgkmcnt(0)
	global_store_dwordx4 v[2:3], v[6:9], off
	v_add_u32_e32 v2, v14, v234
	v_or_b32_e32 v39, 24, v36
	s_addc_u32 s3, s5, s3
	ds_read_b128 v[2:5], v2 offset:51200
	v_lshlrev_b32_e32 v6, 11, v38
	v_mov_b32_e32 v7, v221
	v_lshlrev_b32_e32 v235, 7, v39
	s_add_u32 s2, s2, s22
	v_lshl_add_u64 v[12:13], v[10:11], 0, v[6:7]
	v_add_u32_e32 v6, v14, v235
	s_addc_u32 s3, s3, 0
	s_lshl_b32 s4, s8, 4
	ds_read_b128 v[6:9], v6 offset:51200
	s_and_b32 s4, s4, 0xfffff000
	s_add_u32 s4, s30, s4
	s_addc_u32 s5, s31, 0
	s_lshr_b32 s9, s8, 2
	s_waitcnt lgkmcnt(1)
	global_store_dwordx4 v[12:13], v[2:5], off
	v_and_or_b32 v0, s9, 48, v1
	s_lshl_b32 s9, s23, 10
	v_lshlrev_b32_e32 v2, 11, v39
	v_mov_b32_e32 v3, v221
	v_lshl_add_u64 v[2:3], v[10:11], 0, v[2:3]
	v_lshlrev_b32_e32 v0, 6, v0
	v_mov_b32_e32 v1, v221
	s_cmp_lg_u32 0, -1
	s_waitcnt lgkmcnt(0)
	global_store_dwordx4 v[2:3], v[6:9], off
	v_lshl_add_u64 v[0:1], s[4:5], 0, v[0:1]
	s_cselect_b32 s4, 0, 0
	s_waitcnt lgkmcnt(0)
	s_barrier
	v_lshlrev_b32_e32 v2, 1, v208
	v_mov_b32_e32 v3, v221
	s_add_i32 s25, s4, s9
	v_lshl_add_u64 v[208:209], v[0:1], 0, v[2:3]
	s_addk_i32 s25, 0x6000
	s_mov_b32 s4, m0
	s_mov_b32 m0, s25
	s_nop 0
	global_load_lds_dwordx4 v[208:209], off
	s_mov_b32 m0, s4
	v_lshlrev_b32_e32 v0, 1, v210
	v_mov_b32_e32 v0, v221
	v_mov_b32_e32 v1, v221
	v_mov_b32_e32 v2, v221
	v_mov_b32_e32 v4, v221
	v_mov_b32_e32 v5, v221
	v_mov_b32_e32 v6, v221
	v_mov_b32_e32 v7, v221
	v_mov_b32_e32 v8, v221
	v_mov_b32_e32 v9, v221
	v_mov_b32_e32 v10, v221
	v_mov_b32_e32 v11, v221
	v_mov_b32_e32 v12, v221
	v_mov_b32_e32 v13, v221
	v_mov_b32_e32 v14, v221
	v_mov_b32_e32 v15, v221
	s_waitcnt vmcnt(5) lgkmcnt(0)
	s_barrier
	ds_read_b128 v[32:35], v224
	s_cmp_lg_u32 s26, 0
	s_waitcnt lgkmcnt(0)
	v_mfma_f32_32x32x16_f16 v[16:31], v[32:35], v[156:159], v[0:15]
	ds_read_b128 v[32:35], v224 offset:512
	s_cselect_b64 s[2:3], -1, 0
	v_lshlrev_b32_e32 v239, 10, v36
	v_lshlrev_b32_e32 v238, 10, v37
	v_lshlrev_b32_e32 v237, 10, v38
	v_lshlrev_b32_e32 v236, 10, v39
	v_or_b32_e32 v221, s12, v222
	s_waitcnt lgkmcnt(0)
	v_mfma_f32_32x32x16_f16 v[0:15], v[32:35], v[156:159], v[0:15]
	ds_read_b128 v[32:35], v224 offset:2048
	s_and_b64 vcc, exec, s[2:3]
	s_waitcnt lgkmcnt(0)
	v_mfma_f32_32x32x16_f16 v[16:31], v[32:35], v[152:155], v[16:31]
	ds_read_b128 v[32:35], v224 offset:2560
	s_waitcnt lgkmcnt(0)
	v_mfma_f32_32x32x16_f16 v[0:15], v[32:35], v[152:155], v[0:15]
	ds_read_b128 v[32:35], v224 offset:4096
	s_waitcnt lgkmcnt(0)
	v_mfma_f32_32x32x16_f16 v[16:31], v[32:35], v[148:151], v[16:31]
	ds_read_b128 v[32:35], v224 offset:4608
	s_waitcnt lgkmcnt(0)
	v_mfma_f32_32x32x16_f16 v[0:15], v[32:35], v[148:151], v[0:15]
	ds_read_b128 v[32:35], v224 offset:6144
	s_waitcnt lgkmcnt(0)
	v_mfma_f32_32x32x16_f16 v[16:31], v[32:35], v[144:147], v[16:31]
	ds_read_b128 v[32:35], v224 offset:6656
	s_waitcnt lgkmcnt(0)
	v_mfma_f32_32x32x16_f16 v[0:15], v[32:35], v[144:147], v[0:15]
	s_nop 15
	s_nop 7
	s_cbranch_vccnz .LBB2_119
	v_readfirstlane_b32 s12, v221
	s_cmp_lt_i32 s12, 0
	s_cbranch_scc1 .LBB2_111
	s_cmp_gt_u32 s12, 31
	s_cbranch_scc1 .LBB2_112
	v_mov_b32_e32 v32, 0xff800000
	v_cmp_lt_u32_e32 vcc, v227, v221
	v_or_b32_e32 v33, 2, v227
	s_mov_b32 s13, 0xff800000
	v_cndmask_b32_e32 v17, v32, v17, vcc
	v_cmp_le_u32_e32 vcc, v227, v221
	s_nop 1
	v_cndmask_b32_e32 v16, v32, v16, vcc
	v_cmp_le_u32_e32 vcc, v33, v221
	v_or_b32_e32 v33, 3, v227
	s_nop 0
	v_cndmask_b32_e32 v18, v32, v18, vcc
	v_cmp_le_u32_e32 vcc, v33, v221
	v_or_b32_e32 v33, 8, v227
	s_nop 0
	v_cndmask_b32_e32 v19, v32, v19, vcc
	v_cmp_le_u32_e32 vcc, v33, v221
	v_or_b32_e32 v33, 9, v227
	s_nop 0
	v_cndmask_b32_e32 v20, v32, v20, vcc
	v_cmp_le_u32_e32 vcc, v33, v221
	v_or_b32_e32 v33, 10, v227
	s_nop 0
	v_cndmask_b32_e32 v21, v32, v21, vcc
	v_cmp_le_u32_e32 vcc, v33, v221
	v_or_b32_e32 v33, 11, v227
	s_nop 0
	v_cndmask_b32_e32 v22, v32, v22, vcc
	v_cmp_le_u32_e32 vcc, v33, v221
	v_or_b32_e32 v33, 16, v227
	s_nop 0
	v_cndmask_b32_e32 v23, v32, v23, vcc
	v_cmp_le_u32_e32 vcc, v33, v221
	v_or_b32_e32 v33, 17, v227
	s_nop 0
	v_cndmask_b32_e32 v24, v32, v24, vcc
	v_cmp_le_u32_e32 vcc, v33, v221
	v_or_b32_e32 v33, 18, v227
	s_nop 0
	v_cndmask_b32_e32 v25, v32, v25, vcc
	v_cmp_le_u32_e32 vcc, v33, v221
	v_or_b32_e32 v33, 19, v227
	s_nop 0
	v_cndmask_b32_e32 v26, v32, v26, vcc
	v_cmp_le_u32_e32 vcc, v33, v221
	v_or_b32_e32 v33, 24, v227
	s_nop 0
	v_cndmask_b32_e32 v27, v32, v27, vcc
	v_cmp_le_u32_e32 vcc, v33, v221
	v_or_b32_e32 v33, 25, v227
	s_nop 0
	v_cndmask_b32_e32 v28, v32, v28, vcc
	v_cmp_le_u32_e32 vcc, v33, v221
	v_or_b32_e32 v33, 26, v227
	s_nop 0
	v_cndmask_b32_e32 v29, v32, v29, vcc
	v_cmp_le_u32_e32 vcc, v33, v221
	s_nop 1
	v_cndmask_b32_e32 v30, v32, v30, vcc
	v_or_b32_e32 v32, 27, v227
	v_cmp_gt_u32_e32 vcc, v32, v221
	s_and_saveexec_b64 s[4:5], vcc
	v_mov_b32_e32 v31, s13
	s_or_b64 exec, exec, s[4:5]
	s_branch .LBB2_112
